# baseline (speedup 1.0000x reference)
.LBB5_72:
	s_or_b64 exec, exec, s[2:3]
	v_lshrrev_b32_e32 v4, 3, v1
	s_ashr_i32 s1, s0, 31
	v_lshlrev_b32_e32 v0, 4, v0
	s_lshl_b32 s2, s0, 1
	v_and_b32_e32 v8, 0x70, v0
	s_lshl_b64 s[0:1], s[0:1], 1
	v_mul_u32_u24_e32 v0, 0x210, v4
	s_add_u32 s0, s10, s0
	v_add3_u32 v14, s2, v8, v0
	s_addc_u32 s1, s11, s1
	v_mov_b32_e32 v9, 0
	ds_read_b128 v[0:3], v14
	v_lshl_add_u64 v[10:11], s[0:1], 0, v[8:9]
	v_or_b32_e32 v8, s48, v4
	v_lshlrev_b64 v[4:5], 9, v[8:9]
	v_lshl_add_u64 v[12:13], v[10:11], 0, v[4:5]
	ds_read_b128 v[4:7], v14 offset:4224
	s_waitcnt lgkmcnt(1)
	global_store_dwordx4 v[12:13], v[0:3], off nt
	s_nop 1
	v_or_b32_e32 v0, 8, v8
	v_mov_b32_e32 v1, v9
	v_lshlrev_b64 v[0:1], 9, v[0:1]
	v_lshl_add_u64 v[0:1], v[10:11], 0, v[0:1]
	s_waitcnt lgkmcnt(0)
	global_store_dwordx4 v[0:1], v[4:7], off nt
	ds_read_b128 v[0:3], v14 offset:8448
	s_nop 0
	v_or_b32_e32 v4, 16, v8
	v_mov_b32_e32 v5, v9
	v_lshlrev_b64 v[4:5], 9, v[4:5]
	v_lshl_add_u64 v[12:13], v[10:11], 0, v[4:5]
	ds_read_b128 v[4:7], v14 offset:12672
	v_or_b32_e32 v8, 24, v8
	s_waitcnt lgkmcnt(1)
	global_store_dwordx4 v[12:13], v[0:3], off nt
	s_nop 1
	v_lshlrev_b64 v[0:1], 9, v[8:9]
	v_lshl_add_u64 v[0:1], v[10:11], 0, v[0:1]
	s_waitcnt lgkmcnt(0)
	global_store_dwordx4 v[0:1], v[4:7], off nt
	s_endpgm
	.p2align	8

.LBB6_7:
	s_lshr_b32 s2, s2, 3
	v_and_b32_e32 v78, 31, v0
	v_lshrrev_b32_e32 v6, 3, v0
	s_lshr_b32 s52, s53, 6
	s_add_i32 s2, s3, s2
	v_lshlrev_b32_e32 v2, 5, v78
	v_mov_b32_e32 v3, 0
	v_and_b32_e32 v7, 4, v6
	v_and_b32_e32 v1, 63, v0
	s_lshl_b32 s33, s2, 5
	s_waitcnt lgkmcnt(0)
	v_lshl_add_u64 v[4:5], s[0:1], 0, v[2:3]
	v_lshlrev_b32_e32 v2, 2, v7
	s_lshl_b32 s54, s52, 3
	v_lshl_add_u64 v[4:5], v[4:5], 0, v[2:3]
	s_add_i32 s55, s33, s54
	v_min_u32_e32 v2, 8, v1
	v_add_u32_e32 v2, s55, v2
	v_lshl_add_u64 v[2:3], v[2:3], 2, s[16:17]
	global_load_dword v80, v[2:3], off
	v_and_b32_e32 v81, 15, v0
	s_mov_b32 s27, 0x20000
	s_mov_b32 s30, 0x67c280
	s_and_b32 s29, s19, 0xffff
	v_or_b32_e32 v82, 16, v81
	s_mov_b32 s0, s18
	s_mov_b32 s1, s29
	s_mov_b32 s2, s30
	s_mov_b32 s3, s27
	v_and_b32_e32 v83, 6, v6
	s_mov_b32 s38, 0xc3500
	s_and_b32 s37, s21, 0xffff
	s_mov_b32 s42, 0x186a00
	s_and_b32 s23, s23, 0xffff
	s_mov_b32 s6, s38
	s_mov_b32 s7, s27
	s_mov_b32 s44, s22
	s_mov_b32 s45, s23
	s_mov_b32 s46, s42
	s_mov_b32 s47, s27
	v_lshlrev_b32_e32 v84, 1, v83
	s_lshl_b32 s17, s55, 4
	v_lshlrev_b32_e32 v88, 4, v78
	v_bfe_u32 v90, v0, 4, 2
	v_lshl_or_b32 v89, v7, 1, v88
	v_lshlrev_b32_e32 v7, 4, v81
	s_and_b32 s25, s25, 0xffff
	s_mov_b32 s31, s27
	s_mov_b32 s39, s27
	s_mov_b32 s36, s20
	s_mov_b32 s43, s27
	s_mov_b32 s56, 0
	s_mov_b32 s40, s22
	s_mov_b32 s41, s23
	v_mov_b32_e32 v14, 0xff800000
	s_waitcnt vmcnt(0)
	v_readlane_b32 s4, v80, 0
	v_readlane_b32 s16, v80, 1
	s_not_b32 s5, s4
	s_add_i32 s5, s16, s5
	v_min_i32_e32 v2, s5, v81
	v_min_i32_e32 v3, s5, v82
	v_add_lshl_u32 v2, v2, s4, 2
	v_add_lshl_u32 v3, v3, s4, 2
	buffer_load_dword v21, v2, s[0:3], 0 offen
	buffer_load_dword v20, v3, s[0:3], 0 offen
	v_readlane_b32 s26, v80, 2
	s_not_b32 s28, s16
	s_add_i32 s26, s26, s28
	v_min_i32_e32 v6, s26, v81
	v_min_i32_e32 v8, s26, v82
	v_add_lshl_u32 v6, v6, s16, 2
	s_mov_b32 s4, s20
	s_mov_b32 s5, s37
	global_load_dwordx4 v[2:5], v[4:5], off
	v_add_lshl_u32 v8, v8, s16, 2
	buffer_load_dword v85, v6, s[0:3], 0 offen
	buffer_load_dword v86, v8, s[0:3], 0 offen
	s_lshl_b32 s0, s52, 9
	s_add_i32 s2, s0, 0x4200
	s_lshl_b32 s0, s52, 7
	s_add_i32 s3, s0, 0x5200
	s_mov_b32 s26, 0x30d4000
	s_mov_b32 s28, s18
	v_cmp_gt_u32_e64 s[0:1], 16, v1
	v_lshl_or_b32 v92, v81, 2, s3
	s_waitcnt vmcnt(4)
	v_lshl_or_b32 v6, v21, 3, v83
	s_waitcnt vmcnt(3)
	v_lshl_or_b32 v8, v20, 3, v83
	buffer_load_ushort v24, v6, s[4:7], 0 offen
	buffer_load_ushort v23, v8, s[4:7], 0 offen
	buffer_load_dword v22, v84, s[44:47], s17 offen
	v_lshlrev_b32_e32 v8, 2, v90
	v_or3_b32 v91, s2, v7, v8
	v_lshlrev_b32_e32 v7, 4, v82
	v_bfe_u32 v6, v0, 3, 2
	v_or3_b32 v93, s2, v7, v8
	v_bfe_u32 v7, v0, 5, 1
	v_lshlrev_b32_e32 v8, 2, v6
	v_lshlrev_b32_e32 v79, 2, v7
	v_lshlrev_b32_e32 v87, 4, v7
	v_or_b32_e32 v94, s3, v79
	v_or3_b32 v95, s2, v87, v8
	v_cmp_gt_u32_e64 s[2:3], 8, v78
	v_cmp_eq_u32_e64 s[4:5], 1, v6
	v_cmp_eq_u32_e64 s[6:7], 2, v6
	s_branch .LBB6_10
.LBB6_8:
	v_mov_b32_e32 v77, 0
	v_mov_b32_e32 v76, v77
	v_mov_b32_e32 v75, v77
	v_mov_b32_e32 v74, v77
	v_mov_b32_e32 v73, v77
	v_mov_b32_e32 v72, v77
	v_mov_b32_e32 v71, v77
	v_mov_b32_e32 v70, v77
.LBB6_9:
	s_nop 1
	v_permlane32_swap_b32 v70, v74
	s_nop 1
	v_permlane32_swap_b32 v71, v75
	s_nop 1
	v_permlane32_swap_b32 v72, v76
	s_nop 1
	v_permlane32_swap_b32 v73, v77
	s_add_i32 s16, s56, s54
	v_pk_add_f32 v[6:7], v[70:71], v[74:75]
	v_pk_add_f32 v[10:11], v[72:73], v[76:77]
	v_pk_add_f32 v[6:7], v[2:3], v[6:7]
	v_pk_add_f32 v[10:11], v[4:5], v[10:11]
	v_mul_f32_e32 v8, 0x3fb8aa3b, v6
	v_mul_f32_e32 v9, 0x3fb8aa3b, v7
	v_exp_f32_e32 v8, v8
	v_exp_f32_e32 v9, v9
	v_cmp_lt_f32_e32 vcc, 0, v7
	s_mulk_i32 s16, 0x210
	s_cmp_eq_u32 s57, 8
	v_pk_add_f32 v[8:9], v[8:9], -1.0 op_sel_hi:[1,0]
	s_waitcnt vmcnt(0)
	v_mov_b32_e32 v22, v19
	v_cndmask_b32_e32 v7, v9, v7, vcc
	v_mul_f32_e32 v9, 0x3fb8aa3b, v10
	v_exp_f32_e32 v12, v9
	v_mul_f32_e32 v9, 0x3fb8aa3b, v11
	v_exp_f32_e32 v13, v9
	v_cmp_lt_f32_e32 vcc, 0, v6
	v_mov_b32_e32 v23, v18
	v_mov_b32_e32 v24, v17
	v_cndmask_b32_e32 v6, v8, v6, vcc
	v_pk_add_f32 v[8:9], v[12:13], -1.0 op_sel_hi:[1,0]
	v_cmp_lt_f32_e32 vcc, 0, v11
	v_cvt_pk_f16_f32 v6, v6, v7
	v_mov_b32_e32 v21, v85
	v_cndmask_b32_e32 v7, v9, v11, vcc
	v_cmp_lt_f32_e32 vcc, 0, v10
	v_mov_b32_e32 v20, v86
	v_mov_b32_e32 v85, v15
	v_cndmask_b32_e32 v8, v8, v10, vcc
	v_cvt_pk_f16_f32 v7, v8, v7
	v_add_u32_e32 v8, s16, v89
	v_mov_b32_e32 v86, v16
	s_mov_b32 s56, s57
	ds_write_b64 v8, v[6:7]
	s_cbranch_scc1 .LBB6_91
.LBB6_10:
	s_min_u32 s16, s56, 5
	s_add_i32 s17, s16, 2
	v_readlane_b32 s17, v80, s17
	s_add_i32 s16, s16, 3
	v_readlane_b32 s16, v80, s16
	s_not_b32 s22, s17
	s_add_i32 s16, s16, s22
	s_add_i32 s57, s56, 1
	v_min_i32_e32 v6, s16, v81
	v_min_i32_e32 v7, s16, v82
	s_min_u32 s16, s57, 7
	v_add_lshl_u32 v6, v6, s17, 2
	s_or_b32 s16, s16, s55
	v_add_lshl_u32 v7, v7, s17, 2
	buffer_load_dword v15, v6, s[28:31], 0 offen
	buffer_load_dword v16, v7, s[28:31], 0 offen
	s_waitcnt vmcnt(6)
	v_lshl_or_b32 v6, v85, 3, v83
	s_lshl_b32 s16, s16, 4
	s_waitcnt vmcnt(5)
	v_lshl_or_b32 v7, v86, 3, v83
	buffer_load_ushort v17, v6, s[36:39], 0 offen
	buffer_load_ushort v18, v7, s[36:39], 0 offen
	buffer_load_dword v19, v84, s[40:43], s16 offen
	v_readlane_b32 s59, v80, s56
	v_readlane_b32 s16, v80, s57
	s_sub_i32 s58, s16, s59
	s_cmp_gt_i32 s58, 32
	s_mov_b64 s[16:17], -1
	s_cbranch_scc0 .LBB6_55
	s_add_i32 s60, s58, -1
	s_mov_b32 s16, 0
	v_mov_b32_e32 v6, 0xff800000
.LBB6_12:
	v_add_u32_e32 v7, s16, v81
	v_min_u32_e32 v8, s60, v7
	v_add_u32_e32 v12, 16, v7
	v_add_u32_e32 v8, s59, v8
	v_min_u32_e32 v10, s60, v12
	v_ashrrev_i32_e32 v9, 31, v8
	v_add_u32_e32 v10, s59, v10
	v_lshl_add_u64 v[8:9], v[8:9], 2, s[18:19]
	v_ashrrev_i32_e32 v11, 31, v10
	global_load_dword v13, v[8:9], off
	v_lshl_add_u64 v[8:9], v[10:11], 2, s[18:19]
	global_load_dword v10, v[8:9], off
	v_cmp_gt_u32_e32 vcc, s58, v7
	s_add_i32 s16, s16, 32
	s_cmp_lt_u32 s16, s58
	s_waitcnt vmcnt(1)
	v_lshl_or_b32 v8, v13, 2, v90
	v_ashrrev_i32_e32 v9, 31, v8
	s_waitcnt vmcnt(0)
	v_lshl_or_b32 v10, v10, 2, v90
	v_lshl_add_u64 v[8:9], v[8:9], 1, s[20:21]
	v_ashrrev_i32_e32 v11, 31, v10
	global_load_ushort v13, v[8:9], off
	v_lshl_add_u64 v[8:9], v[10:11], 1, s[20:21]
	global_load_ushort v8, v[8:9], off
	s_waitcnt vmcnt(1)
	v_cvt_f32_f16_e32 v9, v13
	s_waitcnt vmcnt(0)
	v_cvt_f32_f16_e32 v8, v8
	v_add_f32_e32 v9, v22, v9
	v_mul_f32_e32 v10, 0x3e4ccccd, v9
	v_add_f32_e32 v8, v22, v8
	v_max3_f32 v9, v6, v9, v10
	v_mul_f32_e32 v10, 0x3e4ccccd, v8
	v_cndmask_b32_e32 v6, v6, v9, vcc
	v_max3_f32 v7, v6, v8, v10
	v_cmp_gt_u32_e32 vcc, s58, v12
	s_nop 1
	v_cndmask_b32_e32 v6, v6, v7, vcc
	s_cbranch_scc1 .LBB6_12
	s_nop 1
	v_max_f32_dpp v6, v6, v6 quad_perm:[1,0,3,2] row_mask:0xf bank_mask:0xf
	v_mov_b32_e32 v25, 0
	s_nop 1
	v_max_f32_dpp v6, v6, v6 quad_perm:[2,3,0,1] row_mask:0xf bank_mask:0xf
	s_mov_b32 s61, 0
	s_mov_b32 s62, s58
	v_mov_b32_e32 v70, 0
	v_mov_b32_e32 v71, v25
	v_mov_b32_e32 v72, v25
	v_mov_b32_e32 v73, v25
	v_mov_b32_e32 v74, v25
	v_mov_b32_e32 v75, v25
	v_mov_b32_e32 v76, v25
	v_mov_b32_e32 v77, v25
	s_nop 1
	v_max_f32_dpp v6, v6, v6 row_half_mirror row_mask:0xf bank_mask:0xf
	s_nop 0
	s_nop 1
	v_max_f32_dpp v26, v6, v6 row_mirror row_mask:0xf bank_mask:0xf
	s_branch .LBB6_15
.LBB6_14:
	s_waitcnt vmcnt(0)
	v_add_f32_e32 v6, v27, v28
	s_add_i32 s61, s61, 32
	s_sub_i32 s62, s62, 32
	s_cmp_lt_u32 s61, s58
	v_add_f32_e32 v25, v25, v6
	s_cbranch_scc0 .LBB6_54
.LBB6_15:
	v_add_u32_e32 v8, s61, v81
	v_min_i32_e32 v6, s60, v8
	v_add_u32_e32 v6, s59, v6
	v_add_u32_e32 v9, 16, v8
	v_ashrrev_i32_e32 v7, 31, v6
	v_lshl_add_u64 v[10:11], v[6:7], 2, s[18:19]
	v_min_i32_e32 v6, s60, v9
	v_add_u32_e32 v6, s59, v6
	v_ashrrev_i32_e32 v7, 31, v6
	v_lshl_add_u64 v[12:13], v[6:7], 2, s[18:19]
	global_load_dword v7, v[10:11], off
	global_load_dword v6, v[12:13], off
	v_cmp_gt_u32_e32 vcc, s58, v8
	v_mov_b32_e32 v8, 0xff800000
	v_mov_b32_e32 v10, 0xff800000
	s_and_saveexec_b64 s[16:17], vcc
	s_cbranch_execz .LBB6_17
	s_waitcnt vmcnt(1)
	v_lshl_or_b32 v10, v7, 2, v90
	v_ashrrev_i32_e32 v11, 31, v10
	v_lshl_add_u64 v[10:11], v[10:11], 1, s[20:21]
	global_load_ushort v10, v[10:11], off
	s_waitcnt vmcnt(0)
	v_cvt_f32_f16_e32 v10, v10
	v_add_f32_e32 v10, v22, v10
	v_mul_f32_e32 v11, 0x3e4ccccd, v10
	v_max_f32_e32 v10, v10, v11
.LBB6_17:
	s_or_b64 exec, exec, s[16:17]
	v_cmp_gt_u32_e32 vcc, s58, v9
	s_and_saveexec_b64 s[16:17], vcc
	s_cbranch_execz .LBB6_19
	s_waitcnt vmcnt(0)
	v_lshl_or_b32 v8, v6, 2, v90
	v_ashrrev_i32_e32 v9, 31, v8
	v_lshl_add_u64 v[8:9], v[8:9], 1, s[20:21]
	global_load_ushort v8, v[8:9], off
	s_waitcnt vmcnt(0)
	v_cvt_f32_f16_e32 v8, v8
	v_add_f32_e32 v8, v22, v8
	v_mul_f32_e32 v9, 0x3e4ccccd, v8
	v_max_f32_e32 v8, v8, v9
.LBB6_19:
	s_or_b64 exec, exec, s[16:17]
	v_sub_f32_e32 v9, v10, v26
	v_mul_f32_e32 v9, 0x3fb8aa3b, v9
	v_exp_f32_e32 v27, v9
	ds_write_b32 v91, v27
	s_and_saveexec_b64 s[16:17], s[0:1]
	s_cbranch_execz .LBB6_21
	s_waitcnt vmcnt(1)
	ds_write_b32 v92, v7
.LBB6_21:
	s_or_b64 exec, exec, s[16:17]
	s_waitcnt vmcnt(1)
	v_sub_f32_e32 v7, v8, v26
	v_mul_f32_e32 v7, 0x3fb8aa3b, v7
	v_exp_f32_e32 v28, v7
	s_cmp_lt_i32 s62, 17
	s_cbranch_scc1 .LBB6_25
	ds_write_b32 v93, v28
	s_and_saveexec_b64 s[16:17], s[0:1]
	s_cbranch_execz .LBB6_24
	s_waitcnt vmcnt(0)
	ds_write_b32 v92, v6 offset:64

.LBB6_25:
	s_min_i32 s16, s62, 32
	s_add_i32 s16, s16, 3
	s_ashr_i32 s63, s16, 2
	s_cmp_lt_i32 s63, 1
	s_cbranch_scc1 .LBB6_14
	s_waitcnt vmcnt(0)
	s_min_u32 s17, s63, 4
	s_lshl_b32 s22, s17, 4
	s_add_i32 s22, s22, -64
	v_add_u32_e32 v38, s22, v94
	s_lshl_b32 s22, s22, 2
	v_add_u32_e32 v39, s22, v95
	ds_read2_b32 v[30:31], v39 offset0:0 offset1:8
	ds_read2_b32 v[32:33], v39 offset0:16 offset1:24
	ds_read2_b32 v[34:35], v39 offset0:32 offset1:40
	ds_read2_b32 v[36:37], v39 offset0:48 offset1:56
	ds_read2_b32 v[6:7], v38 offset0:0 offset1:2
	ds_read2_b32 v[8:9], v38 offset0:4 offset1:6
	ds_read2_b32 v[10:11], v38 offset0:8 offset1:10
	ds_read2_b32 v[12:13], v38 offset0:12 offset1:14
	s_waitcnt lgkmcnt(0)
	s_cmp_eq_u32 s17, 1
	s_cbranch_scc1 .Lagg1g_b0_i0
	s_cmp_eq_u32 s17, 2
	s_cbranch_scc1 .Lagg1g_b0_i1
	s_cmp_eq_u32 s17, 3
	s_cbranch_scc1 .Lagg1g_b0_i2
	v_lshl_or_b32 v6, v6, 9, v88
	v_lshl_or_b32 v7, v7, 9, v88
	buffer_load_dwordx4 v[66:69], v6, s[24:27], 0 offen sc0 sc1
	buffer_load_dwordx4 v[62:65], v7, s[24:27], 0 offen sc0 sc1
.Lagg1g_b0_i2:
	v_lshl_or_b32 v8, v8, 9, v88
	v_lshl_or_b32 v9, v9, 9, v88
	buffer_load_dwordx4 v[58:61], v8, s[24:27], 0 offen sc0 sc1
	buffer_load_dwordx4 v[54:57], v9, s[24:27], 0 offen sc0 sc1
.Lagg1g_b0_i1:
	v_lshl_or_b32 v10, v10, 9, v88
	v_lshl_or_b32 v11, v11, 9, v88
	buffer_load_dwordx4 v[50:53], v10, s[24:27], 0 offen sc0 sc1
	buffer_load_dwordx4 v[46:49], v11, s[24:27], 0 offen sc0 sc1
.Lagg1g_b0_i0:
	v_lshl_or_b32 v12, v12, 9, v88
	v_lshl_or_b32 v13, v13, 9, v88
	buffer_load_dwordx4 v[42:45], v12, s[24:27], 0 offen sc0 sc1
	buffer_load_dwordx4 v[38:41], v13, s[24:27], 0 offen sc0 sc1
	s_cmp_eq_u32 s17, 1
	s_cbranch_scc1 .Lagg1g_b0_f0
	s_cmp_eq_u32 s17, 2
	s_cbranch_scc1 .Lagg1g_b0_f1
	s_cmp_eq_u32 s17, 3
	s_cbranch_scc1 .Lagg1g_b0_f2
	s_waitcnt vmcnt(7)
	v_fma_mix_f32 v70, v30, v66, v70 op_sel_hi:[0,1,0]
	v_fma_mix_f32 v71, v30, v66, v71 op_sel:[0,1,0] op_sel_hi:[0,1,0]
	v_fma_mix_f32 v72, v30, v67, v72 op_sel_hi:[0,1,0]
	v_fma_mix_f32 v73, v30, v67, v73 op_sel:[0,1,0] op_sel_hi:[0,1,0]
	v_fma_mix_f32 v74, v30, v68, v74 op_sel_hi:[0,1,0]
	v_fma_mix_f32 v75, v30, v68, v75 op_sel:[0,1,0] op_sel_hi:[0,1,0]
	v_fma_mix_f32 v76, v30, v69, v76 op_sel_hi:[0,1,0]
	v_fma_mix_f32 v77, v30, v69, v77 op_sel:[0,1,0] op_sel_hi:[0,1,0]
	s_waitcnt vmcnt(6)
	v_fma_mix_f32 v70, v31, v62, v70 op_sel_hi:[0,1,0]
	v_fma_mix_f32 v71, v31, v62, v71 op_sel:[0,1,0] op_sel_hi:[0,1,0]
	v_fma_mix_f32 v72, v31, v63, v72 op_sel_hi:[0,1,0]
	v_fma_mix_f32 v73, v31, v63, v73 op_sel:[0,1,0] op_sel_hi:[0,1,0]
	v_fma_mix_f32 v74, v31, v64, v74 op_sel_hi:[0,1,0]
	v_fma_mix_f32 v75, v31, v64, v75 op_sel:[0,1,0] op_sel_hi:[0,1,0]
	v_fma_mix_f32 v76, v31, v65, v76 op_sel_hi:[0,1,0]
	v_fma_mix_f32 v77, v31, v65, v77 op_sel:[0,1,0] op_sel_hi:[0,1,0]
.Lagg1g_b0_f2:
	s_waitcnt vmcnt(5)
	v_fma_mix_f32 v70, v32, v58, v70 op_sel_hi:[0,1,0]
	v_fma_mix_f32 v71, v32, v58, v71 op_sel:[0,1,0] op_sel_hi:[0,1,0]
	v_fma_mix_f32 v72, v32, v59, v72 op_sel_hi:[0,1,0]
	v_fma_mix_f32 v73, v32, v59, v73 op_sel:[0,1,0] op_sel_hi:[0,1,0]
	v_fma_mix_f32 v74, v32, v60, v74 op_sel_hi:[0,1,0]
	v_fma_mix_f32 v75, v32, v60, v75 op_sel:[0,1,0] op_sel_hi:[0,1,0]
	v_fma_mix_f32 v76, v32, v61, v76 op_sel_hi:[0,1,0]
	v_fma_mix_f32 v77, v32, v61, v77 op_sel:[0,1,0] op_sel_hi:[0,1,0]
	s_waitcnt vmcnt(4)
	v_fma_mix_f32 v70, v33, v54, v70 op_sel_hi:[0,1,0]
	v_fma_mix_f32 v71, v33, v54, v71 op_sel:[0,1,0] op_sel_hi:[0,1,0]
	v_fma_mix_f32 v72, v33, v55, v72 op_sel_hi:[0,1,0]
	v_fma_mix_f32 v73, v33, v55, v73 op_sel:[0,1,0] op_sel_hi:[0,1,0]
	v_fma_mix_f32 v74, v33, v56, v74 op_sel_hi:[0,1,0]
	v_fma_mix_f32 v75, v33, v56, v75 op_sel:[0,1,0] op_sel_hi:[0,1,0]
	v_fma_mix_f32 v76, v33, v57, v76 op_sel_hi:[0,1,0]
	v_fma_mix_f32 v77, v33, v57, v77 op_sel:[0,1,0] op_sel_hi:[0,1,0]
.Lagg1g_b0_f1:
	s_waitcnt vmcnt(3)
	v_fma_mix_f32 v70, v34, v50, v70 op_sel_hi:[0,1,0]
	v_fma_mix_f32 v71, v34, v50, v71 op_sel:[0,1,0] op_sel_hi:[0,1,0]
	v_fma_mix_f32 v72, v34, v51, v72 op_sel_hi:[0,1,0]
	v_fma_mix_f32 v73, v34, v51, v73 op_sel:[0,1,0] op_sel_hi:[0,1,0]
	v_fma_mix_f32 v74, v34, v52, v74 op_sel_hi:[0,1,0]
	v_fma_mix_f32 v75, v34, v52, v75 op_sel:[0,1,0] op_sel_hi:[0,1,0]
	v_fma_mix_f32 v76, v34, v53, v76 op_sel_hi:[0,1,0]
	v_fma_mix_f32 v77, v34, v53, v77 op_sel:[0,1,0] op_sel_hi:[0,1,0]
	s_waitcnt vmcnt(2)
	v_fma_mix_f32 v70, v35, v46, v70 op_sel_hi:[0,1,0]
	v_fma_mix_f32 v71, v35, v46, v71 op_sel:[0,1,0] op_sel_hi:[0,1,0]
	v_fma_mix_f32 v72, v35, v47, v72 op_sel_hi:[0,1,0]
	v_fma_mix_f32 v73, v35, v47, v73 op_sel:[0,1,0] op_sel_hi:[0,1,0]
	v_fma_mix_f32 v74, v35, v48, v74 op_sel_hi:[0,1,0]
	v_fma_mix_f32 v75, v35, v48, v75 op_sel:[0,1,0] op_sel_hi:[0,1,0]
	v_fma_mix_f32 v76, v35, v49, v76 op_sel_hi:[0,1,0]
	v_fma_mix_f32 v77, v35, v49, v77 op_sel:[0,1,0] op_sel_hi:[0,1,0]
.Lagg1g_b0_f0:
	s_waitcnt vmcnt(1)
	v_fma_mix_f32 v70, v36, v42, v70 op_sel_hi:[0,1,0]
	v_fma_mix_f32 v71, v36, v42, v71 op_sel:[0,1,0] op_sel_hi:[0,1,0]
	v_fma_mix_f32 v72, v36, v43, v72 op_sel_hi:[0,1,0]
	v_fma_mix_f32 v73, v36, v43, v73 op_sel:[0,1,0] op_sel_hi:[0,1,0]
	v_fma_mix_f32 v74, v36, v44, v74 op_sel_hi:[0,1,0]
	v_fma_mix_f32 v75, v36, v44, v75 op_sel:[0,1,0] op_sel_hi:[0,1,0]
	v_fma_mix_f32 v76, v36, v45, v76 op_sel_hi:[0,1,0]
	v_fma_mix_f32 v77, v36, v45, v77 op_sel:[0,1,0] op_sel_hi:[0,1,0]
	s_waitcnt vmcnt(0)
	v_fma_mix_f32 v70, v37, v38, v70 op_sel_hi:[0,1,0]
	v_fma_mix_f32 v71, v37, v38, v71 op_sel:[0,1,0] op_sel_hi:[0,1,0]
	v_fma_mix_f32 v72, v37, v39, v72 op_sel_hi:[0,1,0]
	v_fma_mix_f32 v73, v37, v39, v73 op_sel:[0,1,0] op_sel_hi:[0,1,0]
	v_fma_mix_f32 v74, v37, v40, v74 op_sel_hi:[0,1,0]
	v_fma_mix_f32 v75, v37, v40, v75 op_sel:[0,1,0] op_sel_hi:[0,1,0]
	v_fma_mix_f32 v76, v37, v41, v76 op_sel_hi:[0,1,0]
	v_fma_mix_f32 v77, v37, v41, v77 op_sel:[0,1,0] op_sel_hi:[0,1,0]
	s_cmp_lt_u32 s63, 5
	s_cbranch_scc1 .Lagg1g_done
	s_add_i32 s17, s63, -4
	s_lshl_b32 s22, s17, 4
	s_add_i32 s22, s22, 0
	v_add_u32_e32 v38, s22, v94
	s_lshl_b32 s22, s22, 2
	v_add_u32_e32 v39, s22, v95
	ds_read2_b32 v[30:31], v39 offset0:0 offset1:8
	ds_read2_b32 v[32:33], v39 offset0:16 offset1:24
	ds_read2_b32 v[34:35], v39 offset0:32 offset1:40
	ds_read2_b32 v[36:37], v39 offset0:48 offset1:56
	ds_read2_b32 v[6:7], v38 offset0:0 offset1:2
	ds_read2_b32 v[8:9], v38 offset0:4 offset1:6
	ds_read2_b32 v[10:11], v38 offset0:8 offset1:10
	ds_read2_b32 v[12:13], v38 offset0:12 offset1:14
	s_waitcnt lgkmcnt(0)
	s_cmp_eq_u32 s17, 1
	s_cbranch_scc1 .Lagg1g_b1_i0
	s_cmp_eq_u32 s17, 2
	s_cbranch_scc1 .Lagg1g_b1_i1
	s_cmp_eq_u32 s17, 3
	s_cbranch_scc1 .Lagg1g_b1_i2
	v_lshl_or_b32 v6, v6, 9, v88
	v_lshl_or_b32 v7, v7, 9, v88
	buffer_load_dwordx4 v[66:69], v6, s[24:27], 0 offen sc0 sc1
	buffer_load_dwordx4 v[62:65], v7, s[24:27], 0 offen sc0 sc1

.Lagg1g_b1_f0:
	s_waitcnt vmcnt(1)
	v_fma_mix_f32 v70, v36, v42, v70 op_sel_hi:[0,1,0]
	v_fma_mix_f32 v71, v36, v42, v71 op_sel:[0,1,0] op_sel_hi:[0,1,0]
	v_fma_mix_f32 v72, v36, v43, v72 op_sel_hi:[0,1,0]
	v_fma_mix_f32 v73, v36, v43, v73 op_sel:[0,1,0] op_sel_hi:[0,1,0]
	v_fma_mix_f32 v74, v36, v44, v74 op_sel_hi:[0,1,0]
	v_fma_mix_f32 v75, v36, v44, v75 op_sel:[0,1,0] op_sel_hi:[0,1,0]
	v_fma_mix_f32 v76, v36, v45, v76 op_sel_hi:[0,1,0]
	v_fma_mix_f32 v77, v36, v45, v77 op_sel:[0,1,0] op_sel_hi:[0,1,0]
	s_waitcnt vmcnt(0)
	v_fma_mix_f32 v70, v37, v38, v70 op_sel_hi:[0,1,0]
	v_fma_mix_f32 v71, v37, v38, v71 op_sel:[0,1,0] op_sel_hi:[0,1,0]
	v_fma_mix_f32 v72, v37, v39, v72 op_sel_hi:[0,1,0]
	v_fma_mix_f32 v73, v37, v39, v73 op_sel:[0,1,0] op_sel_hi:[0,1,0]
	v_fma_mix_f32 v74, v37, v40, v74 op_sel_hi:[0,1,0]
	v_fma_mix_f32 v75, v37, v40, v75 op_sel:[0,1,0] op_sel_hi:[0,1,0]
	v_fma_mix_f32 v76, v37, v41, v76 op_sel_hi:[0,1,0]
	v_fma_mix_f32 v77, v37, v41, v77 op_sel:[0,1,0] op_sel_hi:[0,1,0]
.Lagg1g_done:
	s_branch .LBB6_14
.LBB6_54:
	s_nop 1
	v_add_f32_dpp v6, v25, v25 quad_perm:[1,0,3,2] row_mask:0xf bank_mask:0xf
	s_nop 0
	s_nop 1
	v_add_f32_dpp v6, v6, v6 quad_perm:[2,3,0,1] row_mask:0xf bank_mask:0xf
	s_nop 0
	s_nop 1
	v_add_f32_dpp v6, v6, v6 row_half_mirror row_mask:0xf bank_mask:0xf
	s_nop 0
	s_nop 1
	v_add_f32_dpp v6, v6, v6 row_mirror row_mask:0xf bank_mask:0xf
	s_nop 0
	v_readlane_b32 s22, v6, 32
	v_readlane_b32 s23, v6, 48
	v_readlane_b32 s16, v6, 0
	v_readlane_b32 s17, v6, 16
	v_mov_b32_e32 v6, s23
	v_mov_b32_e32 v7, s22
	v_cndmask_b32_e64 v6, v6, v7, s[6:7]
	v_mov_b32_e32 v7, s17
	v_cndmask_b32_e64 v6, v6, v7, s[4:5]
	v_mov_b32_e32 v7, s16
	v_cndmask_b32_e64 v6, v6, v7, s[2:3]
	v_rcp_f32_e32 v6, v6
	s_mov_b64 s[16:17], 0
	v_pk_mul_f32 v[76:77], v[6:7], v[76:77] op_sel_hi:[0,1]
	v_pk_mul_f32 v[74:75], v[6:7], v[74:75] op_sel_hi:[0,1]
	v_pk_mul_f32 v[72:73], v[6:7], v[72:73] op_sel_hi:[0,1]
	v_pk_mul_f32 v[70:71], v[6:7], v[70:71] op_sel_hi:[0,1]
.LBB6_55:
	s_and_b64 vcc, exec, s[16:17]
	s_cbranch_vccz .LBB6_9
	s_waitcnt vmcnt(7)
	v_cvt_f32_f16_e32 v6, v24
	s_waitcnt vmcnt(6)
	v_cvt_f32_f16_e32 v7, v23
	v_cmp_gt_i32_e32 vcc, s58, v81
	s_waitcnt vmcnt(5)
	v_add_f32_e32 v6, v22, v6
	v_add_f32_e32 v7, v22, v7
	v_mul_f32_e32 v8, 0x3e4ccccd, v6
	v_max_f32_e32 v6, v6, v8
	v_mul_f32_e32 v8, 0x3e4ccccd, v7
	v_cndmask_b32_e32 v6, v14, v6, vcc
	v_max_f32_e32 v7, v7, v8
	v_cmp_gt_i32_e32 vcc, s58, v82
	s_nop 1
	v_cndmask_b32_e32 v7, v14, v7, vcc
	v_max_f32_e32 v8, v6, v7
	s_nop 1
	v_max_f32_dpp v8, v8, v8 quad_perm:[1,0,3,2] row_mask:0xf bank_mask:0xf
	s_nop 0
	s_nop 1
	v_max_f32_dpp v8, v8, v8 quad_perm:[2,3,0,1] row_mask:0xf bank_mask:0xf
	s_nop 0
	s_nop 1
	v_max_f32_dpp v8, v8, v8 row_half_mirror row_mask:0xf bank_mask:0xf
	s_nop 0
	s_nop 1
	v_max_f32_dpp v8, v8, v8 row_mirror row_mask:0xf bank_mask:0xf
	s_nop 0
	v_sub_f32_e32 v6, v6, v8
	v_mul_f32_e32 v6, 0x3fb8aa3b, v6
	v_exp_f32_e32 v9, v6
	v_sub_f32_e32 v6, v7, v8
	v_mul_f32_e32 v6, 0x3fb8aa3b, v6
	v_exp_f32_e32 v6, v6
	s_nop 0
	v_add_f32_e32 v7, v9, v6
	s_nop 1
	v_add_f32_dpp v7, v7, v7 quad_perm:[1,0,3,2] row_mask:0xf bank_mask:0xf
	s_nop 0
	s_nop 1
	v_add_f32_dpp v7, v7, v7 quad_perm:[2,3,0,1] row_mask:0xf bank_mask:0xf
	s_nop 0
	s_nop 1
	v_add_f32_dpp v7, v7, v7 row_half_mirror row_mask:0xf bank_mask:0xf
	s_nop 0
	s_nop 1
	v_add_f32_dpp v7, v7, v7 row_mirror row_mask:0xf bank_mask:0xf
	s_nop 0
	v_rcp_f32_e32 v7, v7
	s_nop 0
	v_mul_f32_e32 v8, v9, v7
	ds_write_b32 v91, v8
	s_and_saveexec_b64 s[16:17], s[0:1]
	ds_write_b32 v92, v21
	s_or_b64 exec, exec, s[16:17]
	s_cmp_lt_i32 s58, 17
	s_cbranch_scc1 .LBB6_62
	v_mul_f32_e32 v6, v6, v7
	ds_write_b32 v93, v6
	s_and_saveexec_b64 s[16:17], s[0:1]
	ds_write_b32 v92, v20 offset:64
	s_or_b64 exec, exec, s[16:17]
.LBB6_62:
	s_add_i32 s58, s58, 3
	s_ashr_i32 s58, s58, 2
	s_cmp_lt_i32 s58, 1
	s_cbranch_scc1 .LBB6_8
	v_mov_b32_e32 v70, 0
	v_mov_b32_e32 v71, 0
	v_mov_b32_e32 v72, 0
	v_mov_b32_e32 v73, 0
	v_mov_b32_e32 v74, 0
	v_mov_b32_e32 v75, 0
	v_mov_b32_e32 v76, 0
	v_mov_b32_e32 v77, 0
	s_min_u32 s17, s58, 4
	s_lshl_b32 s22, s17, 4
	s_add_i32 s22, s22, -64
	v_add_u32_e32 v38, s22, v94
	s_lshl_b32 s22, s22, 2
	v_add_u32_e32 v39, s22, v95
	ds_read2_b32 v[30:31], v39 offset0:0 offset1:8
	ds_read2_b32 v[32:33], v39 offset0:16 offset1:24
	ds_read2_b32 v[34:35], v39 offset0:32 offset1:40
	ds_read2_b32 v[36:37], v39 offset0:48 offset1:56
	ds_read2_b32 v[6:7], v38 offset0:0 offset1:2
	ds_read2_b32 v[8:9], v38 offset0:4 offset1:6
	ds_read2_b32 v[10:11], v38 offset0:8 offset1:10
	ds_read2_b32 v[12:13], v38 offset0:12 offset1:14
	s_waitcnt lgkmcnt(0)
	s_cmp_eq_u32 s17, 1
	s_cbranch_scc1 .Lagg1f_b0_i0
	s_cmp_eq_u32 s17, 2
	s_cbranch_scc1 .Lagg1f_b0_i1
	s_cmp_eq_u32 s17, 3
	s_cbranch_scc1 .Lagg1f_b0_i2
	v_lshl_or_b32 v6, v6, 9, v88
	v_lshl_or_b32 v7, v7, 9, v88
	buffer_load_dwordx4 v[66:69], v6, s[24:27], 0 offen sc0 sc1
	buffer_load_dwordx4 v[62:65], v7, s[24:27], 0 offen sc0 sc1

.Lagg1f_b0_f0:
	s_waitcnt vmcnt(1)
	v_fma_mix_f32 v70, v36, v42, v70 op_sel_hi:[0,1,0]
	v_fma_mix_f32 v71, v36, v42, v71 op_sel:[0,1,0] op_sel_hi:[0,1,0]
	v_fma_mix_f32 v72, v36, v43, v72 op_sel_hi:[0,1,0]
	v_fma_mix_f32 v73, v36, v43, v73 op_sel:[0,1,0] op_sel_hi:[0,1,0]
	v_fma_mix_f32 v74, v36, v44, v74 op_sel_hi:[0,1,0]
	v_fma_mix_f32 v75, v36, v44, v75 op_sel:[0,1,0] op_sel_hi:[0,1,0]
	v_fma_mix_f32 v76, v36, v45, v76 op_sel_hi:[0,1,0]
	v_fma_mix_f32 v77, v36, v45, v77 op_sel:[0,1,0] op_sel_hi:[0,1,0]
	s_waitcnt vmcnt(0)
	v_fma_mix_f32 v70, v37, v38, v70 op_sel_hi:[0,1,0]
	v_fma_mix_f32 v71, v37, v38, v71 op_sel:[0,1,0] op_sel_hi:[0,1,0]
	v_fma_mix_f32 v72, v37, v39, v72 op_sel_hi:[0,1,0]
	v_fma_mix_f32 v73, v37, v39, v73 op_sel:[0,1,0] op_sel_hi:[0,1,0]
	v_fma_mix_f32 v74, v37, v40, v74 op_sel_hi:[0,1,0]
	v_fma_mix_f32 v75, v37, v40, v75 op_sel:[0,1,0] op_sel_hi:[0,1,0]
	v_fma_mix_f32 v76, v37, v41, v76 op_sel_hi:[0,1,0]
	v_fma_mix_f32 v77, v37, v41, v77 op_sel:[0,1,0] op_sel_hi:[0,1,0]
	s_cmp_lt_u32 s58, 5
	s_cbranch_scc1 .Lagg1f_done
	s_add_i32 s17, s58, -4
	s_lshl_b32 s22, s17, 4
	s_add_i32 s22, s22, 0
	v_add_u32_e32 v38, s22, v94
	s_lshl_b32 s22, s22, 2
	v_add_u32_e32 v39, s22, v95
	ds_read2_b32 v[30:31], v39 offset0:0 offset1:8
	ds_read2_b32 v[32:33], v39 offset0:16 offset1:24
	ds_read2_b32 v[34:35], v39 offset0:32 offset1:40
	ds_read2_b32 v[36:37], v39 offset0:48 offset1:56
	ds_read2_b32 v[6:7], v38 offset0:0 offset1:2
	ds_read2_b32 v[8:9], v38 offset0:4 offset1:6
	ds_read2_b32 v[10:11], v38 offset0:8 offset1:10
	ds_read2_b32 v[12:13], v38 offset0:12 offset1:14
	s_waitcnt lgkmcnt(0)
	s_cmp_eq_u32 s17, 1
	s_cbranch_scc1 .Lagg1f_b1_i0
	s_cmp_eq_u32 s17, 2
	s_cbranch_scc1 .Lagg1f_b1_i1
	s_cmp_eq_u32 s17, 3
	s_cbranch_scc1 .Lagg1f_b1_i2
	v_lshl_or_b32 v6, v6, 9, v88
	v_lshl_or_b32 v7, v7, 9, v88
	buffer_load_dwordx4 v[66:69], v6, s[24:27], 0 offen sc0 sc1
	buffer_load_dwordx4 v[62:65], v7, s[24:27], 0 offen sc0 sc1

.LBB6_95:
	s_or_b64 exec, exec, s[2:3]
	v_lshrrev_b32_e32 v4, 3, v1
	s_ashr_i32 s1, s0, 31
	v_lshlrev_b32_e32 v0, 4, v0
	s_lshl_b32 s2, s0, 1
	v_and_b32_e32 v8, 0x70, v0
	s_lshl_b64 s[0:1], s[0:1], 1
	v_mul_u32_u24_e32 v0, 0x210, v4
	s_add_u32 s0, s10, s0
	v_add3_u32 v14, s2, v8, v0
	s_addc_u32 s1, s11, s1
	v_mov_b32_e32 v9, 0
	ds_read_b128 v[0:3], v14
	v_lshl_add_u64 v[10:11], s[0:1], 0, v[8:9]
	v_or_b32_e32 v8, s33, v4
	v_lshlrev_b64 v[4:5], 9, v[8:9]
	v_lshl_add_u64 v[12:13], v[10:11], 0, v[4:5]
	ds_read_b128 v[4:7], v14 offset:4224
	s_waitcnt lgkmcnt(1)
	global_store_dwordx4 v[12:13], v[0:3], off nt
	s_nop 1
	v_or_b32_e32 v0, 8, v8
	v_mov_b32_e32 v1, v9
	v_lshlrev_b64 v[0:1], 9, v[0:1]
	v_lshl_add_u64 v[0:1], v[10:11], 0, v[0:1]
	s_waitcnt lgkmcnt(0)
	global_store_dwordx4 v[0:1], v[4:7], off nt
	ds_read_b128 v[0:3], v14 offset:8448
	s_nop 0
	v_or_b32_e32 v4, 16, v8
	v_mov_b32_e32 v5, v9
	v_lshlrev_b64 v[4:5], 9, v[4:5]
	v_lshl_add_u64 v[12:13], v[10:11], 0, v[4:5]
	ds_read_b128 v[4:7], v14 offset:12672
	v_or_b32_e32 v8, 24, v8
	s_waitcnt lgkmcnt(1)
	global_store_dwordx4 v[12:13], v[0:3], off nt
	s_nop 1
	v_lshlrev_b64 v[0:1], 9, v[8:9]
	v_lshl_add_u64 v[0:1], v[10:11], 0, v[0:1]
	s_waitcnt lgkmcnt(0)
	global_store_dwordx4 v[0:1], v[4:7], off nt
	s_endpgm
	.p2align	8

	.amdhsa_kernel _Z7k_layerILi1EEvPKiS1_PKfS3_PKDF16_S3_S5_S5_PDF16_P15HIP_vector_typeIfLj4EES9_S3_S3_S3_S3_S3_S3_PfSA_
		.amdhsa_group_segment_fixed_size 21504
		.amdhsa_private_segment_fixed_size 0
		.amdhsa_kernarg_size 152
		.amdhsa_user_sgpr_count 2
		.amdhsa_user_sgpr_dispatch_ptr 0
		.amdhsa_user_sgpr_queue_ptr 0
		.amdhsa_user_sgpr_kernarg_segment_ptr 1
		.amdhsa_user_sgpr_dispatch_id 0
		.amdhsa_user_sgpr_kernarg_preload_length 0
		.amdhsa_user_sgpr_kernarg_preload_offset 0
		.amdhsa_user_sgpr_private_segment_size 0
		.amdhsa_uses_dynamic_stack 0
		.amdhsa_enable_private_segment 0
		.amdhsa_system_sgpr_workgroup_id_x 1
		.amdhsa_system_sgpr_workgroup_id_y 0
		.amdhsa_system_sgpr_workgroup_id_z 0
		.amdhsa_system_sgpr_workgroup_info 0
		.amdhsa_system_vgpr_workitem_id 0
		.amdhsa_next_free_vgpr 96
		.amdhsa_next_free_sgpr 75
		.amdhsa_accum_offset 96
		.amdhsa_reserve_vcc 1
		.amdhsa_float_round_mode_32 0
		.amdhsa_float_round_mode_16_64 0
		.amdhsa_float_denorm_mode_32 3
		.amdhsa_float_denorm_mode_16_64 3
		.amdhsa_dx10_clamp 1
		.amdhsa_ieee_mode 1
		.amdhsa_fp16_overflow 0
		.amdhsa_tg_split 0
		.amdhsa_exception_fp_ieee_invalid_op 0
		.amdhsa_exception_fp_denorm_src 0
		.amdhsa_exception_fp_ieee_div_zero 0
		.amdhsa_exception_fp_ieee_overflow 0
		.amdhsa_exception_fp_ieee_underflow 0
		.amdhsa_exception_fp_ieee_inexact 0
		.amdhsa_exception_int_div_zero 0
	.end_amdhsa_kernel

.LBB7_98:
	s_endpgm
	.p2align	8

amdhsa.kernels:
  - .agpr_count:     0
    .args:
      - .actual_access:  read_only
        .address_space:  global
        .offset:         0
        .size:           8
        .value_kind:     global_buffer
      - .actual_access:  write_only
        .address_space:  global
        .offset:         8
        .size:           8
        .value_kind:     global_buffer
      - .actual_access:  read_only
        .address_space:  global
        .offset:         16
        .size:           8
        .value_kind:     global_buffer
      - .actual_access:  read_only
        .address_space:  global
        .offset:         24
        .size:           8
        .value_kind:     global_buffer
      - .actual_access:  read_only
        .address_space:  global
        .offset:         32
        .size:           8
        .value_kind:     global_buffer
      - .actual_access:  read_only
        .address_space:  global
        .offset:         40
        .size:           8
        .value_kind:     global_buffer
      - .actual_access:  read_only
        .address_space:  global
        .offset:         48
        .size:           8
        .value_kind:     global_buffer
      - .actual_access:  read_only
        .address_space:  global
        .offset:         56
        .size:           8
        .value_kind:     global_buffer
      - .actual_access:  read_only
        .address_space:  global
        .offset:         64
        .size:           8
        .value_kind:     global_buffer
      - .actual_access:  read_only
        .address_space:  global
        .offset:         72
        .size:           8
        .value_kind:     global_buffer
      - .actual_access:  read_only
        .address_space:  global
        .offset:         80
        .size:           8
        .value_kind:     global_buffer
      - .actual_access:  write_only
        .address_space:  global
        .offset:         88
        .size:           8
        .value_kind:     global_buffer
      - .actual_access:  write_only
        .address_space:  global
        .offset:         96
        .size:           8
        .value_kind:     global_buffer
      - .actual_access:  write_only
        .address_space:  global
        .offset:         104
        .size:           8
        .value_kind:     global_buffer
      - .actual_access:  write_only
        .address_space:  global
        .offset:         112
        .size:           8
        .value_kind:     global_buffer
      - .actual_access:  write_only
        .address_space:  global
        .offset:         120
        .size:           8
        .value_kind:     global_buffer
    .group_segment_fixed_size: 1564
    .kernarg_segment_align: 8
    .kernarg_segment_size: 128
    .language:       OpenCL C
    .language_version:
      - 2
      - 0
    .max_flat_workgroup_size: 1024
    .name:           _Z6k_pre1PKiPiPKfS3_S3_S3_S3_S3_S3_S3_S3_PDF16_S4_S4_PfS5_
    .private_segment_fixed_size: 0
    .sgpr_count:     22
    .sgpr_spill_count: 0
    .symbol:         _Z6k_pre1PKiPiPKfS3_S3_S3_S3_S3_S3_S3_S3_PDF16_S4_S4_PfS5_.kd
    .uniform_work_group_size: 1
    .uses_dynamic_stack: false
    .vgpr_count:     66
    .vgpr_spill_count: 0
    .wavefront_size: 64
  - .agpr_count:     0
    .args:
      - .actual_access:  read_only
        .address_space:  global
        .offset:         0
        .size:           8
        .value_kind:     global_buffer
      - .actual_access:  read_only
        .address_space:  global
        .offset:         8
        .size:           8
        .value_kind:     global_buffer
      - .actual_access:  read_only
        .address_space:  global
        .offset:         16
        .size:           8
        .value_kind:     global_buffer
      - .actual_access:  read_only
        .address_space:  global
        .offset:         24
        .size:           8
        .value_kind:     global_buffer
      - .actual_access:  write_only
        .address_space:  global
        .offset:         32
        .size:           8
        .value_kind:     global_buffer
      - .actual_access:  write_only
        .address_space:  global
        .offset:         40
        .size:           8
        .value_kind:     global_buffer
    .group_segment_fixed_size: 1632
    .kernarg_segment_align: 8
    .kernarg_segment_size: 48
    .language:       OpenCL C
    .language_version:
      - 2
      - 0
    .max_flat_workgroup_size: 1024
    .name:           _Z9k_scatterPKiS0_S0_S0_PiS1_
    .private_segment_fixed_size: 0
    .sgpr_count:     16
    .sgpr_spill_count: 0
    .symbol:         _Z9k_scatterPKiS0_S0_S0_PiS1_.kd
    .uniform_work_group_size: 1
    .uses_dynamic_stack: false
    .vgpr_count:     50
    .vgpr_spill_count: 0
    .wavefront_size: 64
  - .agpr_count:     0
    .args:
      - .actual_access:  read_only
        .address_space:  global
        .offset:         0
        .size:           8
        .value_kind:     global_buffer
      - .actual_access:  read_only
        .address_space:  global
        .offset:         8
        .size:           8
        .value_kind:     global_buffer
      - .actual_access:  write_only
        .address_space:  global
        .offset:         16
        .size:           8
        .value_kind:     global_buffer
      - .actual_access:  write_only
        .address_space:  global
        .offset:         24
        .size:           8
        .value_kind:     global_buffer
      - .actual_access:  read_only
        .address_space:  global
        .offset:         32
        .size:           8
        .value_kind:     global_buffer
      - .actual_access:  read_only
        .address_space:  global
        .offset:         40
        .size:           8
        .value_kind:     global_buffer
      - .actual_access:  read_only
        .address_space:  global
        .offset:         48
        .size:           8
        .value_kind:     global_buffer
      - .actual_access:  read_only
        .address_space:  global
        .offset:         56
        .size:           8
        .value_kind:     global_buffer
      - .actual_access:  write_only
        .address_space:  global
        .offset:         64
        .size:           8
        .value_kind:     global_buffer
      - .actual_access:  write_only
        .address_space:  global
        .offset:         72
        .size:           8
        .value_kind:     global_buffer
      - .actual_access:  write_only
        .address_space:  global
        .offset:         80
        .size:           8
        .value_kind:     global_buffer
    .group_segment_fixed_size: 5952
    .kernarg_segment_align: 8
    .kernarg_segment_size: 88
    .language:       OpenCL C
    .language_version:
      - 2
      - 0
    .max_flat_workgroup_size: 1024
    .name:           _Z5k_csrPKiS0_PiS1_PKfS3_S3_S3_PDF16_P15HIP_vector_typeIfLj4EES7_
    .private_segment_fixed_size: 0
    .sgpr_count:     33
    .sgpr_spill_count: 0
    .symbol:         _Z5k_csrPKiS0_PiS1_PKfS3_S3_S3_PDF16_P15HIP_vector_typeIfLj4EES7_.kd
    .uniform_work_group_size: 1
    .uses_dynamic_stack: false
    .vgpr_count:     116
    .vgpr_spill_count: 0
    .wavefront_size: 64
  - .agpr_count:     0
    .args:
      - .actual_access:  read_only
        .address_space:  global
        .offset:         0
        .size:           8
        .value_kind:     global_buffer
      - .actual_access:  write_only
        .address_space:  global
        .offset:         8
        .size:           8
        .value_kind:     global_buffer
      - .actual_access:  write_only
        .address_space:  global
        .offset:         16
        .size:           8
        .value_kind:     global_buffer
    .group_segment_fixed_size: 16
    .kernarg_segment_align: 8
    .kernarg_segment_size: 24
    .language:       OpenCL C
    .language_version:
      - 2
      - 0
    .max_flat_workgroup_size: 256
    .name:           _Z6k_pre2PKiPiS1_
    .private_segment_fixed_size: 0
    .sgpr_count:     14
    .sgpr_spill_count: 0
    .symbol:         _Z6k_pre2PKiPiS1_.kd
    .uniform_work_group_size: 1
    .uses_dynamic_stack: false
    .vgpr_count:     14
    .vgpr_spill_count: 0
    .wavefront_size: 64
  - .agpr_count:     0
    .args:
      - .actual_access:  read_only
        .address_space:  global
        .offset:         0
        .size:           8
        .value_kind:     global_buffer
      - .actual_access:  read_only
        .address_space:  global
        .offset:         8
        .size:           8
        .value_kind:     global_buffer
      - .actual_access:  read_only
        .address_space:  global
        .offset:         16
        .size:           8
        .value_kind:     global_buffer
      - .actual_access:  read_only
        .address_space:  global
        .offset:         24
        .size:           8
        .value_kind:     global_buffer
      - .actual_access:  read_only
        .address_space:  global
        .offset:         32
        .size:           8
        .value_kind:     global_buffer
      - .actual_access:  write_only
        .address_space:  global
        .offset:         40
        .size:           8
        .value_kind:     global_buffer
    .group_segment_fixed_size: 1408
    .kernarg_segment_align: 8
    .kernarg_segment_size: 48
    .language:       OpenCL C
    .language_version:
      - 2
      - 0
    .max_flat_workgroup_size: 256
    .name:           _Z7k_finalPKfS0_S0_S0_S0_Pf
    .private_segment_fixed_size: 0
    .sgpr_count:     14
    .sgpr_spill_count: 0
    .symbol:         _Z7k_finalPKfS0_S0_S0_S0_Pf.kd
    .uniform_work_group_size: 1
    .uses_dynamic_stack: false
    .vgpr_count:     29
    .vgpr_spill_count: 0
    .wavefront_size: 64
  - .agpr_count:     0
    .args:
      - .actual_access:  read_only
        .address_space:  global
        .offset:         0
        .size:           8
        .value_kind:     global_buffer
      - .actual_access:  read_only
        .address_space:  global
        .offset:         8
        .size:           8
        .value_kind:     global_buffer
      - .actual_access:  read_only
        .address_space:  global
        .offset:         16
        .size:           8
        .value_kind:     global_buffer
      - .actual_access:  read_only
        .address_space:  global
        .offset:         24
        .size:           8
        .value_kind:     global_buffer
      - .actual_access:  read_only
        .address_space:  global
        .offset:         32
        .size:           8
        .value_kind:     global_buffer
      - .actual_access:  read_only
        .address_space:  global
        .offset:         40
        .size:           8
        .value_kind:     global_buffer
      - .actual_access:  read_only
        .address_space:  global
        .offset:         48
        .size:           8
        .value_kind:     global_buffer
      - .actual_access:  read_only
        .address_space:  global
        .offset:         56
        .size:           8
        .value_kind:     global_buffer
      - .actual_access:  write_only
        .address_space:  global
        .offset:         64
        .size:           8
        .value_kind:     global_buffer
      - .actual_access:  write_only
        .address_space:  global
        .offset:         72
        .size:           8
        .value_kind:     global_buffer
      - .actual_access:  write_only
        .address_space:  global
        .offset:         80
        .size:           8
        .value_kind:     global_buffer
      - .actual_access:  read_only
        .address_space:  global
        .offset:         88
        .size:           8
        .value_kind:     global_buffer
      - .actual_access:  read_only
        .address_space:  global
        .offset:         96
        .size:           8
        .value_kind:     global_buffer
      - .actual_access:  read_only
        .address_space:  global
        .offset:         104
        .size:           8
        .value_kind:     global_buffer
      - .actual_access:  read_only
        .address_space:  global
        .offset:         112
        .size:           8
        .value_kind:     global_buffer
      - .actual_access:  read_only
        .address_space:  global
        .offset:         120
        .size:           8
        .value_kind:     global_buffer
      - .actual_access:  read_only
        .address_space:  global
        .offset:         128
        .size:           8
        .value_kind:     global_buffer
      - .actual_access:  read_only
        .address_space:  global
        .offset:         136
        .size:           8
        .value_kind:     global_buffer
      - .actual_access:  read_only
        .address_space:  global
        .offset:         144
        .size:           8
        .value_kind:     global_buffer
    .group_segment_fixed_size: 29248
    .kernarg_segment_align: 8
    .kernarg_segment_size: 152
    .language:       OpenCL C
    .language_version:
      - 2
      - 0
    .max_flat_workgroup_size: 256
    .name:           _Z7k_layerILi0EEvPKiS1_PKfS3_PKDF16_S3_S5_S5_PDF16_P15HIP_vector_typeIfLj4EES9_S3_S3_S3_S3_S3_S3_PfSA_
    .private_segment_fixed_size: 0
    .sgpr_count:     66
    .sgpr_spill_count: 0
    .symbol:         _Z7k_layerILi0EEvPKiS1_PKfS3_PKDF16_S3_S5_S5_PDF16_P15HIP_vector_typeIfLj4EES9_S3_S3_S3_S3_S3_S3_PfSA_.kd
    .uniform_work_group_size: 1
    .uses_dynamic_stack: false
    .vgpr_count:     86
    .vgpr_spill_count: 0
    .wavefront_size: 64
  - .agpr_count:     0
    .args:
      - .actual_access:  read_only
        .address_space:  global
        .offset:         0
        .size:           8
        .value_kind:     global_buffer
      - .actual_access:  read_only
        .address_space:  global
        .offset:         8
        .size:           8
        .value_kind:     global_buffer
      - .actual_access:  read_only
        .address_space:  global
        .offset:         16
        .size:           8
        .value_kind:     global_buffer
      - .actual_access:  read_only
        .address_space:  global
        .offset:         24
        .size:           8
        .value_kind:     global_buffer
      - .actual_access:  read_only
        .address_space:  global
        .offset:         32
        .size:           8
        .value_kind:     global_buffer
      - .actual_access:  read_only
        .address_space:  global
        .offset:         40
        .size:           8
        .value_kind:     global_buffer
      - .actual_access:  read_only
        .address_space:  global
        .offset:         48
        .size:           8
        .value_kind:     global_buffer
      - .actual_access:  read_only
        .address_space:  global
        .offset:         56
        .size:           8
        .value_kind:     global_buffer
      - .actual_access:  write_only
        .address_space:  global
        .offset:         64
        .size:           8
        .value_kind:     global_buffer
      - .actual_access:  write_only
        .address_space:  global
        .offset:         72
        .size:           8
        .value_kind:     global_buffer
      - .actual_access:  write_only
        .address_space:  global
        .offset:         80
        .size:           8
        .value_kind:     global_buffer
      - .actual_access:  read_only
        .address_space:  global
        .offset:         88
        .size:           8
        .value_kind:     global_buffer
      - .actual_access:  read_only
        .address_space:  global
        .offset:         96
        .size:           8
        .value_kind:     global_buffer
      - .actual_access:  read_only
        .address_space:  global
        .offset:         104
        .size:           8
        .value_kind:     global_buffer
      - .actual_access:  read_only
        .address_space:  global
        .offset:         112
        .size:           8
        .value_kind:     global_buffer
      - .actual_access:  read_only
        .address_space:  global
        .offset:         120
        .size:           8
        .value_kind:     global_buffer
      - .actual_access:  read_only
        .address_space:  global
        .offset:         128
        .size:           8
        .value_kind:     global_buffer
      - .actual_access:  read_only
        .address_space:  global
        .offset:         136
        .size:           8
        .value_kind:     global_buffer
      - .actual_access:  read_only
        .address_space:  global
        .offset:         144
        .size:           8
        .value_kind:     global_buffer
    .group_segment_fixed_size: 21504
    .kernarg_segment_align: 8
    .kernarg_segment_size: 152
    .language:       OpenCL C
    .language_version:
      - 2
      - 0
    .max_flat_workgroup_size: 256
    .name:           _Z7k_layerILi1EEvPKiS1_PKfS3_PKDF16_S3_S5_S5_PDF16_P15HIP_vector_typeIfLj4EES9_S3_S3_S3_S3_S3_S3_PfSA_
    .private_segment_fixed_size: 0
    .sgpr_count:     70
    .sgpr_spill_count: 0
    .symbol:         _Z7k_layerILi1EEvPKiS1_PKfS3_PKDF16_S3_S5_S5_PDF16_P15HIP_vector_typeIfLj4EES9_S3_S3_S3_S3_S3_S3_PfSA_.kd
    .uniform_work_group_size: 1
    .uses_dynamic_stack: false
    .vgpr_count:     96
    .vgpr_spill_count: 0
    .wavefront_size: 64
  - .agpr_count:     0
    .args:
      - .actual_access:  read_only
        .address_space:  global
        .offset:         0
        .size:           8
        .value_kind:     global_buffer
      - .actual_access:  read_only
        .address_space:  global
        .offset:         8
        .size:           8
        .value_kind:     global_buffer
      - .actual_access:  read_only
        .address_space:  global
        .offset:         16
        .size:           8
        .value_kind:     global_buffer
      - .actual_access:  read_only
        .address_space:  global
        .offset:         24
        .size:           8
        .value_kind:     global_buffer
      - .actual_access:  read_only
        .address_space:  global
        .offset:         32
        .size:           8
        .value_kind:     global_buffer
      - .actual_access:  read_only
        .address_space:  global
        .offset:         40
        .size:           8
        .value_kind:     global_buffer
      - .actual_access:  read_only
        .address_space:  global
        .offset:         48
        .size:           8
        .value_kind:     global_buffer
      - .actual_access:  read_only
        .address_space:  global
        .offset:         56
        .size:           8
        .value_kind:     global_buffer
      - .actual_access:  read_only
        .address_space:  global
        .offset:         64
        .size:           8
        .value_kind:     global_buffer
      - .actual_access:  read_only
        .address_space:  global
        .offset:         72
        .size:           8
        .value_kind:     global_buffer
      - .actual_access:  read_only
        .address_space:  global
        .offset:         80
        .size:           8
        .value_kind:     global_buffer
      - .actual_access:  read_only
        .address_space:  global
        .offset:         88
        .size:           8
        .value_kind:     global_buffer
      - .actual_access:  read_only
        .address_space:  global
        .offset:         96
        .size:           8
        .value_kind:     global_buffer
      - .actual_access:  read_only
        .address_space:  global
        .offset:         104
        .size:           8
        .value_kind:     global_buffer
      - .actual_access:  read_only
        .address_space:  global
        .offset:         112
        .size:           8
        .value_kind:     global_buffer
      - .actual_access:  read_only
        .address_space:  global
        .offset:         120
        .size:           8
        .value_kind:     global_buffer
      - .actual_access:  read_only
        .address_space:  global
        .offset:         128
        .size:           8
        .value_kind:     global_buffer
      - .actual_access:  write_only
        .address_space:  global
        .offset:         136
        .size:           8
        .value_kind:     global_buffer
      - .address_space:  global
        .offset:         144
        .size:           8
        .value_kind:     global_buffer
    .group_segment_fixed_size: 19456
    .kernarg_segment_align: 8
    .kernarg_segment_size: 152
    .language:       OpenCL C
    .language_version:
      - 2
      - 0
    .max_flat_workgroup_size: 256
    .name:           _Z7k_layerILi2EEvPKiS1_PKfS3_PKDF16_S3_S5_S5_PDF16_P15HIP_vector_typeIfLj4EES9_S3_S3_S3_S3_S3_S3_PfSA_
    .private_segment_fixed_size: 0
    .sgpr_count:     74
    .sgpr_spill_count: 0
    .symbol:         _Z7k_layerILi2EEvPKiS1_PKfS3_PKDF16_S3_S5_S5_PDF16_P15HIP_vector_typeIfLj4EES9_S3_S3_S3_S3_S3_S3_PfSA_.kd
    .uniform_work_group_size: 1
    .uses_dynamic_stack: false
    .vgpr_count:     110
    .vgpr_spill_count: 0
    .wavefront_size: 64
